# P5 EpiOut hand-written: ga/msc loaded once, x loads 2 steps ahead with counted vmcnt
# baseline (speedup 1.0000x reference)
.LBB0_684:
	ds_read_b128 v[142:145], v148
	ds_read_b128 v[152:155], v148 offset:1024
	ds_read_b128 v[156:159], v148 offset:2048
	ds_read_b128 v[160:163], v148 offset:3072
	ds_read_b128 v[164:167], v149
	ds_read_b128 v[168:171], v149 offset:1024
	ds_read_b128 v[172:175], v149 offset:2048
	ds_read_b128 v[176:179], v149 offset:3072
	s_add_u32 s28, s26, 0xfffc0080
	s_addc_u32 s29, s27, -1
	s_cmp_eq_u32 s55, 12
	s_cselect_b32 s31, s17, s29
	s_cselect_b32 s30, s49, s28
	s_cselect_b32 s29, s15, s54
	s_cselect_b32 s28, s52, s53
	v_lshl_add_u64 v[146:147], s[26:27], 0, v[138:139]
	s_add_i32 m0, s25, 0xc000
	ds_read_b128 v[180:183], v150
	ds_read_b128 v[184:187], v150 offset:1024
	ds_read_b128 v[188:191], v150 offset:2048
	ds_read_b128 v[192:195], v150 offset:3072
	ds_read_b128 v[196:199], v150 offset:4096
	ds_read_b128 v[200:203], v150 offset:5120
	ds_read_b128 v[204:207], v150 offset:6144
	ds_read_b128 v[208:211], v150 offset:7168
	global_load_lds_dwordx4 v[146:147], off
	v_lshl_add_u64 v[146:147], s[26:27], 0, v[140:141]
	s_add_i32 m0, s25, 0xe000
	s_nop 0
	global_load_lds_dwordx4 v[146:147], off
	s_waitcnt vmcnt(8)
	s_waitcnt lgkmcnt(0)
	s_barrier
	s_setprio 1
	s_waitcnt lgkmcnt(0)
	v_mfma_i32_16x16x64_i8 v[126:129], v[142:145], v[180:183], v[126:129]
	v_mfma_i32_16x16x64_i8 v[122:125], v[156:159], v[180:183], v[122:125]
	v_mfma_i32_16x16x64_i8 v[110:113], v[142:145], v[188:191], v[110:113]
	v_mfma_i32_16x16x64_i8 v[106:109], v[156:159], v[188:191], v[106:109]
	v_mfma_i32_16x16x64_i8 v[94:97], v[142:145], v[196:199], v[94:97]
	v_mfma_i32_16x16x64_i8 v[90:93], v[156:159], v[196:199], v[90:93]
	v_mfma_i32_16x16x64_i8 v[78:81], v[142:145], v[204:207], v[78:81]
	v_mfma_i32_16x16x64_i8 v[74:77], v[156:159], v[204:207], v[74:77]
	v_mfma_i32_16x16x64_i8 v[126:129], v[152:155], v[184:187], v[126:129]
	v_mfma_i32_16x16x64_i8 v[122:125], v[160:163], v[184:187], v[122:125]
	v_mfma_i32_16x16x64_i8 v[110:113], v[152:155], v[192:195], v[110:113]
	v_mfma_i32_16x16x64_i8 v[106:109], v[160:163], v[192:195], v[106:109]
	v_mfma_i32_16x16x64_i8 v[94:97], v[152:155], v[200:203], v[94:97]
	v_mfma_i32_16x16x64_i8 v[90:93], v[160:163], v[200:203], v[90:93]
	v_mfma_i32_16x16x64_i8 v[78:81], v[152:155], v[208:211], v[78:81]
	v_mfma_i32_16x16x64_i8 v[74:77], v[160:163], v[208:211], v[74:77]
	s_setprio 0
	s_setprio 1
	v_mfma_i32_16x16x64_i8 v[118:121], v[164:167], v[180:183], v[118:121]
	v_mfma_i32_16x16x64_i8 v[114:117], v[172:175], v[180:183], v[114:117]
	v_mfma_i32_16x16x64_i8 v[102:105], v[164:167], v[188:191], v[102:105]
	v_mfma_i32_16x16x64_i8 v[98:101], v[172:175], v[188:191], v[98:101]
	v_mfma_i32_16x16x64_i8 v[86:89], v[164:167], v[196:199], v[86:89]
	v_mfma_i32_16x16x64_i8 v[82:85], v[172:175], v[196:199], v[82:85]
	v_mfma_i32_16x16x64_i8 v[70:73], v[164:167], v[204:207], v[70:73]
	v_mfma_i32_16x16x64_i8 v[66:69], v[172:175], v[204:207], v[66:69]
	v_mfma_i32_16x16x64_i8 v[118:121], v[168:171], v[184:187], v[118:121]
	v_mfma_i32_16x16x64_i8 v[114:117], v[176:179], v[184:187], v[114:117]
	v_mfma_i32_16x16x64_i8 v[102:105], v[168:171], v[192:195], v[102:105]
	v_mfma_i32_16x16x64_i8 v[98:101], v[176:179], v[192:195], v[98:101]
	v_mfma_i32_16x16x64_i8 v[86:89], v[168:171], v[200:203], v[86:89]
	v_mfma_i32_16x16x64_i8 v[82:85], v[176:179], v[200:203], v[82:85]
	v_mfma_i32_16x16x64_i8 v[70:73], v[168:171], v[208:211], v[70:73]
	v_mfma_i32_16x16x64_i8 v[66:69], v[176:179], v[208:211], v[66:69]
	s_setprio 0
	s_barrier
	s_add_i32 s56, s47, s39
	v_lshl_add_u64 v[146:147], s[28:29], 0, v[132:133]
	s_mov_b32 m0, s56
	ds_read_b128 v[180:183], v150 offset:16384
	ds_read_b128 v[184:187], v150 offset:17408
	ds_read_b128 v[188:191], v150 offset:18432
	ds_read_b128 v[192:195], v150 offset:19456
	ds_read_b128 v[196:199], v150 offset:20480
	ds_read_b128 v[200:203], v150 offset:21504
	ds_read_b128 v[204:207], v150 offset:22528
	ds_read_b128 v[208:211], v150 offset:23552
	global_load_lds_dwordx4 v[146:147], off
	s_add_i32 m0, s56, 0x2000
	s_add_u32 s56, s28, 0x40000
	v_lshl_add_u64 v[212:213], s[28:29], 0, v[136:137]
	s_addc_u32 s57, s29, 0
	s_add_i32 s58, s48, s39
	global_load_lds_dwordx4 v[212:213], off
	v_lshl_add_u64 v[216:217], s[56:57], 0, v[132:133]
	s_mov_b32 m0, s58
	v_lshl_add_u64 v[218:219], s[30:31], 0, v[134:135]
	global_load_lds_dwordx4 v[216:217], off
	v_lshl_add_u64 v[216:217], s[56:57], 0, v[136:137]
	s_add_i32 m0, s58, 0x2000
	s_nop 0
	global_load_lds_dwordx4 v[216:217], off
	v_lshl_add_u64 v[216:217], s[30:31], 0, v[130:131]
	s_mov_b32 m0, s25
	s_nop 0
	global_load_lds_dwordx4 v[216:217], off
	s_mov_b32 m0, s40
	s_nop 0
	global_load_lds_dwordx4 v[218:219], off
	s_waitcnt vmcnt(8)
	s_waitcnt lgkmcnt(0)
	s_barrier
	s_setprio 1
	s_waitcnt lgkmcnt(0)
	v_mfma_i32_16x16x64_i8 v[62:65], v[142:145], v[180:183], v[62:65]
	v_mfma_i32_16x16x64_i8 v[58:61], v[156:159], v[180:183], v[58:61]
	v_mfma_i32_16x16x64_i8 v[46:49], v[142:145], v[188:191], v[46:49]
	v_mfma_i32_16x16x64_i8 v[42:45], v[156:159], v[188:191], v[42:45]
	v_mfma_i32_16x16x64_i8 v[30:33], v[142:145], v[196:199], v[30:33]
	v_mfma_i32_16x16x64_i8 v[26:29], v[156:159], v[196:199], v[26:29]
	v_mfma_i32_16x16x64_i8 v[14:17], v[142:145], v[204:207], v[14:17]
	v_mfma_i32_16x16x64_i8 v[10:13], v[156:159], v[204:207], v[10:13]
	v_mfma_i32_16x16x64_i8 v[62:65], v[152:155], v[184:187], v[62:65]
	v_mfma_i32_16x16x64_i8 v[58:61], v[160:163], v[184:187], v[58:61]
	v_mfma_i32_16x16x64_i8 v[46:49], v[152:155], v[192:195], v[46:49]
	v_mfma_i32_16x16x64_i8 v[42:45], v[160:163], v[192:195], v[42:45]
	v_mfma_i32_16x16x64_i8 v[30:33], v[152:155], v[200:203], v[30:33]
	v_mfma_i32_16x16x64_i8 v[26:29], v[160:163], v[200:203], v[26:29]
	v_mfma_i32_16x16x64_i8 v[14:17], v[152:155], v[208:211], v[14:17]
	v_mfma_i32_16x16x64_i8 v[10:13], v[160:163], v[208:211], v[10:13]
	s_setprio 0
	s_setprio 1
	v_mfma_i32_16x16x64_i8 v[54:57], v[164:167], v[180:183], v[54:57]
	v_mfma_i32_16x16x64_i8 v[50:53], v[172:175], v[180:183], v[50:53]
	v_mfma_i32_16x16x64_i8 v[38:41], v[164:167], v[188:191], v[38:41]
	v_mfma_i32_16x16x64_i8 v[34:37], v[172:175], v[188:191], v[34:37]
	v_mfma_i32_16x16x64_i8 v[22:25], v[164:167], v[196:199], v[22:25]
	v_mfma_i32_16x16x64_i8 v[18:21], v[172:175], v[196:199], v[18:21]
	v_mfma_i32_16x16x64_i8 v[6:9], v[164:167], v[204:207], v[6:9]
	v_mfma_i32_16x16x64_i8 v[2:5], v[172:175], v[204:207], v[2:5]
	v_mfma_i32_16x16x64_i8 v[54:57], v[168:171], v[184:187], v[54:57]
	v_mfma_i32_16x16x64_i8 v[50:53], v[176:179], v[184:187], v[50:53]
	v_mfma_i32_16x16x64_i8 v[38:41], v[168:171], v[192:195], v[38:41]
	v_mfma_i32_16x16x64_i8 v[34:37], v[176:179], v[192:195], v[34:37]
	v_mfma_i32_16x16x64_i8 v[22:25], v[168:171], v[200:203], v[22:25]
	v_mfma_i32_16x16x64_i8 v[18:21], v[176:179], v[200:203], v[18:21]
	v_mfma_i32_16x16x64_i8 v[6:9], v[168:171], v[208:211], v[6:9]
	v_mfma_i32_16x16x64_i8 v[2:5], v[176:179], v[208:211], v[2:5]
	s_setprio 0
	s_barrier
	s_add_i32 s56, 0, 0x18000
	s_add_i32 s57, 0, 0x1c000
	v_add_u32_e32 v160, s56, v1
	v_add_u32_e32 v176, s57, v1
	ds_read_b128 v[142:145], v160
	ds_read_b128 v[152:155], v160 offset:1024
	ds_read_b128 v[156:159], v160 offset:2048
	ds_read_b128 v[160:163], v160 offset:3072
	ds_read_b128 v[164:167], v176
	ds_read_b128 v[168:171], v176 offset:1024
	ds_read_b128 v[172:175], v176 offset:2048
	ds_read_b128 v[176:179], v176 offset:3072
	s_add_u32 s30, s30, 0x40000
	s_addc_u32 s31, s31, 0
	s_mov_b32 m0, s41
	v_lshl_add_u64 v[220:221], s[30:31], 0, v[130:131]
	ds_read_b128 v[180:183], v150 offset:32768
	ds_read_b128 v[184:187], v150 offset:33792
	ds_read_b128 v[188:191], v150 offset:34816
	ds_read_b128 v[192:195], v150 offset:35840
	ds_read_b128 v[196:199], v150 offset:36864
	ds_read_b128 v[200:203], v150 offset:37888
	ds_read_b128 v[204:207], v150 offset:38912
	ds_read_b128 v[208:211], v150 offset:39936
	global_load_lds_dwordx4 v[220:221], off
	v_lshl_add_u64 v[220:221], s[30:31], 0, v[134:135]
	s_mov_b32 m0, s42
	s_nop 0
	global_load_lds_dwordx4 v[220:221], off
	s_waitcnt vmcnt(8)
	s_waitcnt lgkmcnt(0)
	s_barrier
	s_setprio 1
	s_waitcnt lgkmcnt(0)
	v_mfma_i32_16x16x64_i8 v[126:129], v[142:145], v[180:183], v[126:129]
	v_mfma_i32_16x16x64_i8 v[122:125], v[156:159], v[180:183], v[122:125]
	v_mfma_i32_16x16x64_i8 v[110:113], v[142:145], v[188:191], v[110:113]
	v_mfma_i32_16x16x64_i8 v[106:109], v[156:159], v[188:191], v[106:109]
	v_mfma_i32_16x16x64_i8 v[94:97], v[142:145], v[196:199], v[94:97]
	v_mfma_i32_16x16x64_i8 v[90:93], v[156:159], v[196:199], v[90:93]
	v_mfma_i32_16x16x64_i8 v[78:81], v[142:145], v[204:207], v[78:81]
	v_mfma_i32_16x16x64_i8 v[74:77], v[156:159], v[204:207], v[74:77]
	v_mfma_i32_16x16x64_i8 v[126:129], v[152:155], v[184:187], v[126:129]
	v_mfma_i32_16x16x64_i8 v[122:125], v[160:163], v[184:187], v[122:125]
	v_mfma_i32_16x16x64_i8 v[110:113], v[152:155], v[192:195], v[110:113]
	v_mfma_i32_16x16x64_i8 v[106:109], v[160:163], v[192:195], v[106:109]
	v_mfma_i32_16x16x64_i8 v[94:97], v[152:155], v[200:203], v[94:97]
	v_mfma_i32_16x16x64_i8 v[90:93], v[160:163], v[200:203], v[90:93]
	v_mfma_i32_16x16x64_i8 v[78:81], v[152:155], v[208:211], v[78:81]
	v_mfma_i32_16x16x64_i8 v[74:77], v[160:163], v[208:211], v[74:77]
	s_setprio 0
	s_setprio 1
	v_mfma_i32_16x16x64_i8 v[118:121], v[164:167], v[180:183], v[118:121]
	v_mfma_i32_16x16x64_i8 v[114:117], v[172:175], v[180:183], v[114:117]
	v_mfma_i32_16x16x64_i8 v[102:105], v[164:167], v[188:191], v[102:105]
	v_mfma_i32_16x16x64_i8 v[98:101], v[172:175], v[188:191], v[98:101]
	v_mfma_i32_16x16x64_i8 v[86:89], v[164:167], v[196:199], v[86:89]
	v_mfma_i32_16x16x64_i8 v[82:85], v[172:175], v[196:199], v[82:85]
	v_mfma_i32_16x16x64_i8 v[70:73], v[164:167], v[204:207], v[70:73]
	v_mfma_i32_16x16x64_i8 v[66:69], v[172:175], v[204:207], v[66:69]
	v_mfma_i32_16x16x64_i8 v[118:121], v[168:171], v[184:187], v[118:121]
	v_mfma_i32_16x16x64_i8 v[114:117], v[176:179], v[184:187], v[114:117]
	v_mfma_i32_16x16x64_i8 v[102:105], v[168:171], v[192:195], v[102:105]
	v_mfma_i32_16x16x64_i8 v[98:101], v[176:179], v[192:195], v[98:101]
	v_mfma_i32_16x16x64_i8 v[86:89], v[168:171], v[200:203], v[86:89]
	v_mfma_i32_16x16x64_i8 v[82:85], v[176:179], v[200:203], v[82:85]
	v_mfma_i32_16x16x64_i8 v[70:73], v[168:171], v[208:211], v[70:73]
	v_mfma_i32_16x16x64_i8 v[66:69], v[176:179], v[208:211], v[66:69]
	s_setprio 0
	s_barrier
	s_add_i32 s30, s56, s39
	v_lshl_add_u64 v[146:147], v[146:147], 0, s[10:11]
	s_mov_b32 m0, s30
	ds_read_b128 v[180:183], v150 offset:49152
	ds_read_b128 v[184:187], v150 offset:50176
	ds_read_b128 v[188:191], v150 offset:51200
	ds_read_b128 v[192:195], v150 offset:52224
	ds_read_b128 v[196:199], v150 offset:53248
	ds_read_b128 v[200:203], v150 offset:54272
	ds_read_b128 v[204:207], v150 offset:55296
	ds_read_b128 v[208:211], v150 offset:56320
	global_load_lds_dwordx4 v[146:147], off
	s_add_i32 m0, s30, 0x2000
	s_add_u32 s28, s28, 0x40080
	v_lshl_add_u64 v[146:147], v[212:213], 0, s[10:11]
	s_addc_u32 s29, s29, 0
	s_add_i32 s30, s57, s39
	global_load_lds_dwordx4 v[146:147], off
	v_lshl_add_u64 v[146:147], s[28:29], 0, v[132:133]
	s_mov_b32 m0, s30
	s_nop 0
	global_load_lds_dwordx4 v[146:147], off
	v_lshl_add_u64 v[146:147], s[28:29], 0, v[136:137]
	s_add_i32 m0, s30, 0x2000
	s_nop 0
	global_load_lds_dwordx4 v[146:147], off
	v_lshl_add_u64 v[146:147], v[216:217], 0, s[10:11]
	s_mov_b32 m0, s45
	s_nop 0
	global_load_lds_dwordx4 v[146:147], off
	v_lshl_add_u64 v[146:147], v[218:219], 0, s[10:11]
	s_mov_b32 m0, s46
	s_nop 0
	global_load_lds_dwordx4 v[146:147], off
	s_waitcnt vmcnt(8)
	s_waitcnt lgkmcnt(0)
	s_barrier
	s_setprio 1
	s_waitcnt lgkmcnt(0)
	v_mfma_i32_16x16x64_i8 v[62:65], v[142:145], v[180:183], v[62:65]
	v_mfma_i32_16x16x64_i8 v[58:61], v[156:159], v[180:183], v[58:61]
	v_mfma_i32_16x16x64_i8 v[46:49], v[142:145], v[188:191], v[46:49]
	v_mfma_i32_16x16x64_i8 v[42:45], v[156:159], v[188:191], v[42:45]
	v_mfma_i32_16x16x64_i8 v[30:33], v[142:145], v[196:199], v[30:33]
	v_mfma_i32_16x16x64_i8 v[26:29], v[156:159], v[196:199], v[26:29]
	v_mfma_i32_16x16x64_i8 v[14:17], v[142:145], v[204:207], v[14:17]
	v_mfma_i32_16x16x64_i8 v[10:13], v[156:159], v[204:207], v[10:13]
	v_mfma_i32_16x16x64_i8 v[62:65], v[152:155], v[184:187], v[62:65]
	v_mfma_i32_16x16x64_i8 v[58:61], v[160:163], v[184:187], v[58:61]
	v_mfma_i32_16x16x64_i8 v[46:49], v[152:155], v[192:195], v[46:49]
	v_mfma_i32_16x16x64_i8 v[42:45], v[160:163], v[192:195], v[42:45]
	v_mfma_i32_16x16x64_i8 v[30:33], v[152:155], v[200:203], v[30:33]
	v_mfma_i32_16x16x64_i8 v[26:29], v[160:163], v[200:203], v[26:29]
	v_mfma_i32_16x16x64_i8 v[14:17], v[152:155], v[208:211], v[14:17]
	v_mfma_i32_16x16x64_i8 v[10:13], v[160:163], v[208:211], v[10:13]
	s_setprio 0
	s_setprio 1
	v_mfma_i32_16x16x64_i8 v[54:57], v[164:167], v[180:183], v[54:57]
	v_mfma_i32_16x16x64_i8 v[50:53], v[172:175], v[180:183], v[50:53]
	v_mfma_i32_16x16x64_i8 v[38:41], v[164:167], v[188:191], v[38:41]
	v_mfma_i32_16x16x64_i8 v[34:37], v[172:175], v[188:191], v[34:37]
	v_mfma_i32_16x16x64_i8 v[22:25], v[164:167], v[196:199], v[22:25]
	v_mfma_i32_16x16x64_i8 v[18:21], v[172:175], v[196:199], v[18:21]
	v_mfma_i32_16x16x64_i8 v[6:9], v[164:167], v[204:207], v[6:9]
	v_mfma_i32_16x16x64_i8 v[2:5], v[172:175], v[204:207], v[2:5]
	v_mfma_i32_16x16x64_i8 v[54:57], v[168:171], v[184:187], v[54:57]
	v_mfma_i32_16x16x64_i8 v[50:53], v[176:179], v[184:187], v[50:53]
	v_mfma_i32_16x16x64_i8 v[38:41], v[168:171], v[192:195], v[38:41]
	v_mfma_i32_16x16x64_i8 v[34:37], v[176:179], v[192:195], v[34:37]
	v_mfma_i32_16x16x64_i8 v[22:25], v[168:171], v[200:203], v[22:25]
	v_mfma_i32_16x16x64_i8 v[18:21], v[176:179], v[200:203], v[18:21]
	v_mfma_i32_16x16x64_i8 v[6:9], v[168:171], v[208:211], v[6:9]
	v_mfma_i32_16x16x64_i8 v[2:5], v[176:179], v[208:211], v[2:5]
	s_setprio 0
	s_barrier
	s_add_i32 s55, s55, 2
	s_add_u32 s26, s26, 0x100
	s_addc_u32 s27, s27, 0
	s_add_u32 s53, s53, 0x100
	s_addc_u32 s54, s54, 0
	s_cmp_gt_u32 s55, 13
	s_cbranch_scc0 .LBB0_684
	s_lshr_b32 s15, s4, 4
	s_mul_i32 s26, s15, 0x3000
	s_ashr_i32 s27, s26, 31
	s_lshl_b64 s[26:27], s[26:27], 2
	s_add_u32 s15, s96, s26
	s_addc_u32 s17, s97, s27
	s_add_u32 s26, s15, 0x104000
	s_addc_u32 s27, s17, 0
	s_lshl_b32 s4, s4, 8
	v_mov_b32_e32 v142, v151
	s_add_i32 s4, s4, s43
	v_and_or_b32 v146, v151, 15, s4
	s_lshl_b32 s15, s24, 8
	s_or_b32 s15, s15, s44
	v_ashrrev_i32_e32 v143, 1, v151
	v_and_b32_e32 v143, -8, v143
	v_add_u32_e32 v142, s15, v143
	v_lshl_add_u32 v144, v146, 11, v142
	v_lshlrev_b32_e32 v248, 2, v144
	v_lshlrev_b32_e32 v249, 1, v144
	v_lshlrev_b32_e32 v250, 2, v146
	v_lshlrev_b32_e32 v251, 2, v142
	global_load_dword v168, v250, s[8:9]
	global_load_dword v169, v250, s[8:9] offset:64
	global_load_dword v170, v250, s[8:9] offset:128
	global_load_dword v171, v250, s[8:9] offset:192
	global_load_dword v172, v250, s[8:9] offset:512
	global_load_dword v173, v250, s[8:9] offset:576
	global_load_dword v174, v250, s[8:9] offset:640
	global_load_dword v175, v250, s[8:9] offset:704
	global_load_dwordx4 v[152:155], v251, s[26:27]
	global_load_dwordx4 v[156:159], v251, s[26:27] offset:16
	global_load_dwordx4 v[160:163], v251, s[26:27] offset:512
	global_load_dwordx4 v[164:167], v251, s[26:27] offset:528
	global_load_dwordx4 v[224:227], v248, s[36:37]
	global_load_dwordx4 v[228:231], v248, s[36:37] offset:16
	global_load_dwordx4 v[232:235], v248, s[36:37] offset:512
	global_load_dwordx4 v[236:239], v248, s[36:37] offset:528
	v_add_u32_e32 v248, 0x20000, v248
	global_load_dwordx4 v[240:243], v248, s[36:37]
	global_load_dwordx4 v[244:247], v248, s[36:37] offset:16
	v_cvt_f32_i32_e32 v126, v126
	v_cvt_f32_i32_e32 v127, v127
	v_cvt_f32_i32_e32 v128, v128
	v_cvt_f32_i32_e32 v129, v129
	v_cvt_f32_i32_e32 v122, v122
	v_cvt_f32_i32_e32 v123, v123
	v_cvt_f32_i32_e32 v124, v124
	v_cvt_f32_i32_e32 v125, v125
	s_waitcnt vmcnt(4)
	v_mul_f32_e32 v222, 0x3a124925, v168
	v_pk_mul_f32 v[126:127], v[222:223], v[126:127] op_sel_hi:[0,1]
	v_pk_mul_f32 v[126:127], v[152:153], v[126:127]
	v_pk_fma_f32 v[126:127], v[224:225], s[12:13], v[126:127] op_sel_hi:[1,0,1]
	v_pk_mul_f32 v[128:129], v[222:223], v[128:129] op_sel_hi:[0,1]
	v_pk_mul_f32 v[128:129], v[154:155], v[128:129]
	v_pk_fma_f32 v[128:129], v[226:227], s[12:13], v[128:129] op_sel_hi:[1,0,1]
	v_pk_mul_f32 v[122:123], v[222:223], v[122:123] op_sel_hi:[0,1]
	v_pk_mul_f32 v[122:123], v[156:157], v[122:123]
	v_pk_fma_f32 v[122:123], v[228:229], s[12:13], v[122:123] op_sel_hi:[1,0,1]
	v_pk_mul_f32 v[124:125], v[222:223], v[124:125] op_sel_hi:[0,1]
	v_pk_mul_f32 v[124:125], v[158:159], v[124:125]
	v_pk_fma_f32 v[124:125], v[230:231], s[12:13], v[124:125] op_sel_hi:[1,0,1]
	v_cvt_pk_bf16_f32 v126, v126, v127
	v_cvt_pk_bf16_f32 v127, v128, v129
	v_cvt_pk_bf16_f32 v128, v122, v123
	v_cvt_pk_bf16_f32 v129, v124, v125
	global_store_dwordx4 v249, v[126:129], s[6:7]
	global_load_dwordx4 v[224:227], v248, s[36:37] offset:512
	global_load_dwordx4 v[228:231], v248, s[36:37] offset:528
	v_cvt_f32_i32_e32 v118, v118
	v_cvt_f32_i32_e32 v119, v119
	v_cvt_f32_i32_e32 v120, v120
	v_cvt_f32_i32_e32 v121, v121
	v_cvt_f32_i32_e32 v114, v114
	v_cvt_f32_i32_e32 v115, v115
	v_cvt_f32_i32_e32 v116, v116
	v_cvt_f32_i32_e32 v117, v117
	s_waitcnt vmcnt(5)
	v_pk_mul_f32 v[118:119], v[222:223], v[118:119] op_sel_hi:[0,1]
	v_pk_mul_f32 v[118:119], v[160:161], v[118:119]
	v_pk_fma_f32 v[118:119], v[232:233], s[12:13], v[118:119] op_sel_hi:[1,0,1]
	v_pk_mul_f32 v[120:121], v[222:223], v[120:121] op_sel_hi:[0,1]
	v_pk_mul_f32 v[120:121], v[162:163], v[120:121]
	v_pk_fma_f32 v[120:121], v[234:235], s[12:13], v[120:121] op_sel_hi:[1,0,1]
	v_pk_mul_f32 v[114:115], v[222:223], v[114:115] op_sel_hi:[0,1]
	v_pk_mul_f32 v[114:115], v[164:165], v[114:115]
	v_pk_fma_f32 v[114:115], v[236:237], s[12:13], v[114:115] op_sel_hi:[1,0,1]
	v_pk_mul_f32 v[116:117], v[222:223], v[116:117] op_sel_hi:[0,1]
	v_pk_mul_f32 v[116:117], v[166:167], v[116:117]
	v_pk_fma_f32 v[116:117], v[238:239], s[12:13], v[116:117] op_sel_hi:[1,0,1]
	v_cvt_pk_bf16_f32 v118, v118, v119
	v_cvt_pk_bf16_f32 v119, v120, v121
	v_cvt_pk_bf16_f32 v120, v114, v115
	v_cvt_pk_bf16_f32 v121, v116, v117
	global_store_dwordx4 v249, v[118:121], s[6:7] offset:256
	v_add_u32_e32 v248, 0x20000, v248
	global_load_dwordx4 v[232:235], v248, s[36:37]
	global_load_dwordx4 v[236:239], v248, s[36:37] offset:16
	v_cvt_f32_i32_e32 v110, v110
	v_cvt_f32_i32_e32 v111, v111
	v_cvt_f32_i32_e32 v112, v112
	v_cvt_f32_i32_e32 v113, v113
	v_cvt_f32_i32_e32 v106, v106
	v_cvt_f32_i32_e32 v107, v107
	v_cvt_f32_i32_e32 v108, v108
	v_cvt_f32_i32_e32 v109, v109
	s_waitcnt vmcnt(6)
	v_mul_f32_e32 v222, 0x3a124925, v169
	v_pk_mul_f32 v[110:111], v[222:223], v[110:111] op_sel_hi:[0,1]
	v_pk_mul_f32 v[110:111], v[152:153], v[110:111]
	v_pk_fma_f32 v[110:111], v[240:241], s[12:13], v[110:111] op_sel_hi:[1,0,1]
	v_pk_mul_f32 v[112:113], v[222:223], v[112:113] op_sel_hi:[0,1]
	v_pk_mul_f32 v[112:113], v[154:155], v[112:113]
	v_pk_fma_f32 v[112:113], v[242:243], s[12:13], v[112:113] op_sel_hi:[1,0,1]
	v_pk_mul_f32 v[106:107], v[222:223], v[106:107] op_sel_hi:[0,1]
	v_pk_mul_f32 v[106:107], v[156:157], v[106:107]
	v_pk_fma_f32 v[106:107], v[244:245], s[12:13], v[106:107] op_sel_hi:[1,0,1]
	v_pk_mul_f32 v[108:109], v[222:223], v[108:109] op_sel_hi:[0,1]
	v_pk_mul_f32 v[108:109], v[158:159], v[108:109]
	v_pk_fma_f32 v[108:109], v[246:247], s[12:13], v[108:109] op_sel_hi:[1,0,1]
	v_cvt_pk_bf16_f32 v110, v110, v111
	v_cvt_pk_bf16_f32 v111, v112, v113
	v_cvt_pk_bf16_f32 v112, v106, v107
	v_cvt_pk_bf16_f32 v113, v108, v109
	v_add_u32_e32 v249, 0x10000, v249
	global_store_dwordx4 v249, v[110:113], s[6:7]
	global_load_dwordx4 v[240:243], v248, s[36:37] offset:512
	global_load_dwordx4 v[244:247], v248, s[36:37] offset:528
	v_cvt_f32_i32_e32 v102, v102
	v_cvt_f32_i32_e32 v103, v103
	v_cvt_f32_i32_e32 v104, v104
	v_cvt_f32_i32_e32 v105, v105
	v_cvt_f32_i32_e32 v98, v98
	v_cvt_f32_i32_e32 v99, v99
	v_cvt_f32_i32_e32 v100, v100
	v_cvt_f32_i32_e32 v101, v101
	s_waitcnt vmcnt(6)
	v_pk_mul_f32 v[102:103], v[222:223], v[102:103] op_sel_hi:[0,1]
	v_pk_mul_f32 v[102:103], v[160:161], v[102:103]
	v_pk_fma_f32 v[102:103], v[224:225], s[12:13], v[102:103] op_sel_hi:[1,0,1]
	v_pk_mul_f32 v[104:105], v[222:223], v[104:105] op_sel_hi:[0,1]
	v_pk_mul_f32 v[104:105], v[162:163], v[104:105]
	v_pk_fma_f32 v[104:105], v[226:227], s[12:13], v[104:105] op_sel_hi:[1,0,1]
	v_pk_mul_f32 v[98:99], v[222:223], v[98:99] op_sel_hi:[0,1]
	v_pk_mul_f32 v[98:99], v[164:165], v[98:99]
	v_pk_fma_f32 v[98:99], v[228:229], s[12:13], v[98:99] op_sel_hi:[1,0,1]
	v_pk_mul_f32 v[100:101], v[222:223], v[100:101] op_sel_hi:[0,1]
	v_pk_mul_f32 v[100:101], v[166:167], v[100:101]
	v_pk_fma_f32 v[100:101], v[230:231], s[12:13], v[100:101] op_sel_hi:[1,0,1]
	v_cvt_pk_bf16_f32 v102, v102, v103
	v_cvt_pk_bf16_f32 v103, v104, v105
	v_cvt_pk_bf16_f32 v104, v98, v99
	v_cvt_pk_bf16_f32 v105, v100, v101
	global_store_dwordx4 v249, v[102:105], s[6:7] offset:256
	v_add_u32_e32 v248, 0x20000, v248
	global_load_dwordx4 v[224:227], v248, s[36:37]
	global_load_dwordx4 v[228:231], v248, s[36:37] offset:16
	v_cvt_f32_i32_e32 v94, v94
	v_cvt_f32_i32_e32 v95, v95
	v_cvt_f32_i32_e32 v96, v96
	v_cvt_f32_i32_e32 v97, v97
	v_cvt_f32_i32_e32 v90, v90
	v_cvt_f32_i32_e32 v91, v91
	v_cvt_f32_i32_e32 v92, v92
	v_cvt_f32_i32_e32 v93, v93
	s_waitcnt vmcnt(6)
	v_mul_f32_e32 v222, 0x3a124925, v170
	v_pk_mul_f32 v[94:95], v[222:223], v[94:95] op_sel_hi:[0,1]
	v_pk_mul_f32 v[94:95], v[152:153], v[94:95]
	v_pk_fma_f32 v[94:95], v[232:233], s[12:13], v[94:95] op_sel_hi:[1,0,1]
	v_pk_mul_f32 v[96:97], v[222:223], v[96:97] op_sel_hi:[0,1]
	v_pk_mul_f32 v[96:97], v[154:155], v[96:97]
	v_pk_fma_f32 v[96:97], v[234:235], s[12:13], v[96:97] op_sel_hi:[1,0,1]
	v_pk_mul_f32 v[90:91], v[222:223], v[90:91] op_sel_hi:[0,1]
	v_pk_mul_f32 v[90:91], v[156:157], v[90:91]
	v_pk_fma_f32 v[90:91], v[236:237], s[12:13], v[90:91] op_sel_hi:[1,0,1]
	v_pk_mul_f32 v[92:93], v[222:223], v[92:93] op_sel_hi:[0,1]
	v_pk_mul_f32 v[92:93], v[158:159], v[92:93]
	v_pk_fma_f32 v[92:93], v[238:239], s[12:13], v[92:93] op_sel_hi:[1,0,1]
	v_cvt_pk_bf16_f32 v94, v94, v95
	v_cvt_pk_bf16_f32 v95, v96, v97
	v_cvt_pk_bf16_f32 v96, v90, v91
	v_cvt_pk_bf16_f32 v97, v92, v93
	v_add_u32_e32 v249, 0x10000, v249
	global_store_dwordx4 v249, v[94:97], s[6:7]
	global_load_dwordx4 v[232:235], v248, s[36:37] offset:512
	global_load_dwordx4 v[236:239], v248, s[36:37] offset:528
	v_cvt_f32_i32_e32 v86, v86
	v_cvt_f32_i32_e32 v87, v87
	v_cvt_f32_i32_e32 v88, v88
	v_cvt_f32_i32_e32 v89, v89
	v_cvt_f32_i32_e32 v82, v82
	v_cvt_f32_i32_e32 v83, v83
	v_cvt_f32_i32_e32 v84, v84
	v_cvt_f32_i32_e32 v85, v85
	s_waitcnt vmcnt(6)
	v_pk_mul_f32 v[86:87], v[222:223], v[86:87] op_sel_hi:[0,1]
	v_pk_mul_f32 v[86:87], v[160:161], v[86:87]
	v_pk_fma_f32 v[86:87], v[240:241], s[12:13], v[86:87] op_sel_hi:[1,0,1]
	v_pk_mul_f32 v[88:89], v[222:223], v[88:89] op_sel_hi:[0,1]
	v_pk_mul_f32 v[88:89], v[162:163], v[88:89]
	v_pk_fma_f32 v[88:89], v[242:243], s[12:13], v[88:89] op_sel_hi:[1,0,1]
	v_pk_mul_f32 v[82:83], v[222:223], v[82:83] op_sel_hi:[0,1]
	v_pk_mul_f32 v[82:83], v[164:165], v[82:83]
	v_pk_fma_f32 v[82:83], v[244:245], s[12:13], v[82:83] op_sel_hi:[1,0,1]
	v_pk_mul_f32 v[84:85], v[222:223], v[84:85] op_sel_hi:[0,1]
	v_pk_mul_f32 v[84:85], v[166:167], v[84:85]
	v_pk_fma_f32 v[84:85], v[246:247], s[12:13], v[84:85] op_sel_hi:[1,0,1]
	v_cvt_pk_bf16_f32 v86, v86, v87
	v_cvt_pk_bf16_f32 v87, v88, v89
	v_cvt_pk_bf16_f32 v88, v82, v83
	v_cvt_pk_bf16_f32 v89, v84, v85
	global_store_dwordx4 v249, v[86:89], s[6:7] offset:256
	v_add_u32_e32 v248, 0xa0000, v248
	global_load_dwordx4 v[240:243], v248, s[36:37]
	global_load_dwordx4 v[244:247], v248, s[36:37] offset:16
	v_cvt_f32_i32_e32 v78, v78
	v_cvt_f32_i32_e32 v79, v79
	v_cvt_f32_i32_e32 v80, v80
	v_cvt_f32_i32_e32 v81, v81
	v_cvt_f32_i32_e32 v74, v74
	v_cvt_f32_i32_e32 v75, v75
	v_cvt_f32_i32_e32 v76, v76
	v_cvt_f32_i32_e32 v77, v77
	s_waitcnt vmcnt(6)
	v_mul_f32_e32 v222, 0x3a124925, v171
	v_pk_mul_f32 v[78:79], v[222:223], v[78:79] op_sel_hi:[0,1]
	v_pk_mul_f32 v[78:79], v[152:153], v[78:79]
	v_pk_fma_f32 v[78:79], v[224:225], s[12:13], v[78:79] op_sel_hi:[1,0,1]
	v_pk_mul_f32 v[80:81], v[222:223], v[80:81] op_sel_hi:[0,1]
	v_pk_mul_f32 v[80:81], v[154:155], v[80:81]
	v_pk_fma_f32 v[80:81], v[226:227], s[12:13], v[80:81] op_sel_hi:[1,0,1]
	v_pk_mul_f32 v[74:75], v[222:223], v[74:75] op_sel_hi:[0,1]
	v_pk_mul_f32 v[74:75], v[156:157], v[74:75]
	v_pk_fma_f32 v[74:75], v[228:229], s[12:13], v[74:75] op_sel_hi:[1,0,1]
	v_pk_mul_f32 v[76:77], v[222:223], v[76:77] op_sel_hi:[0,1]
	v_pk_mul_f32 v[76:77], v[158:159], v[76:77]
	v_pk_fma_f32 v[76:77], v[230:231], s[12:13], v[76:77] op_sel_hi:[1,0,1]
	v_cvt_pk_bf16_f32 v78, v78, v79
	v_cvt_pk_bf16_f32 v79, v80, v81
	v_cvt_pk_bf16_f32 v80, v74, v75
	v_cvt_pk_bf16_f32 v81, v76, v77
	v_add_u32_e32 v249, 0x10000, v249
	global_store_dwordx4 v249, v[78:81], s[6:7]
	global_load_dwordx4 v[224:227], v248, s[36:37] offset:512
	global_load_dwordx4 v[228:231], v248, s[36:37] offset:528
	v_cvt_f32_i32_e32 v70, v70
	v_cvt_f32_i32_e32 v71, v71
	v_cvt_f32_i32_e32 v72, v72
	v_cvt_f32_i32_e32 v73, v73
	v_cvt_f32_i32_e32 v66, v66
	v_cvt_f32_i32_e32 v67, v67
	v_cvt_f32_i32_e32 v68, v68
	v_cvt_f32_i32_e32 v69, v69
	s_waitcnt vmcnt(6)
	v_pk_mul_f32 v[70:71], v[222:223], v[70:71] op_sel_hi:[0,1]
	v_pk_mul_f32 v[70:71], v[160:161], v[70:71]
	v_pk_fma_f32 v[70:71], v[232:233], s[12:13], v[70:71] op_sel_hi:[1,0,1]
	v_pk_mul_f32 v[72:73], v[222:223], v[72:73] op_sel_hi:[0,1]
	v_pk_mul_f32 v[72:73], v[162:163], v[72:73]
	v_pk_fma_f32 v[72:73], v[234:235], s[12:13], v[72:73] op_sel_hi:[1,0,1]
	v_pk_mul_f32 v[66:67], v[222:223], v[66:67] op_sel_hi:[0,1]
	v_pk_mul_f32 v[66:67], v[164:165], v[66:67]
	v_pk_fma_f32 v[66:67], v[236:237], s[12:13], v[66:67] op_sel_hi:[1,0,1]
	v_pk_mul_f32 v[68:69], v[222:223], v[68:69] op_sel_hi:[0,1]
	v_pk_mul_f32 v[68:69], v[166:167], v[68:69]
	v_pk_fma_f32 v[68:69], v[238:239], s[12:13], v[68:69] op_sel_hi:[1,0,1]
	v_cvt_pk_bf16_f32 v70, v70, v71
	v_cvt_pk_bf16_f32 v71, v72, v73
	v_cvt_pk_bf16_f32 v72, v66, v67
	v_cvt_pk_bf16_f32 v73, v68, v69
	global_store_dwordx4 v249, v[70:73], s[6:7] offset:256
	v_add_u32_e32 v248, 0x20000, v248
	global_load_dwordx4 v[232:235], v248, s[36:37]
	global_load_dwordx4 v[236:239], v248, s[36:37] offset:16
	v_cvt_f32_i32_e32 v62, v62
	v_cvt_f32_i32_e32 v63, v63
	v_cvt_f32_i32_e32 v64, v64
	v_cvt_f32_i32_e32 v65, v65
	v_cvt_f32_i32_e32 v58, v58
	v_cvt_f32_i32_e32 v59, v59
	v_cvt_f32_i32_e32 v60, v60
	v_cvt_f32_i32_e32 v61, v61
	s_waitcnt vmcnt(6)
	v_mul_f32_e32 v222, 0x3a124925, v172
	v_pk_mul_f32 v[62:63], v[222:223], v[62:63] op_sel_hi:[0,1]
	v_pk_mul_f32 v[62:63], v[152:153], v[62:63]
	v_pk_fma_f32 v[62:63], v[240:241], s[12:13], v[62:63] op_sel_hi:[1,0,1]
	v_pk_mul_f32 v[64:65], v[222:223], v[64:65] op_sel_hi:[0,1]
	v_pk_mul_f32 v[64:65], v[154:155], v[64:65]
	v_pk_fma_f32 v[64:65], v[242:243], s[12:13], v[64:65] op_sel_hi:[1,0,1]
	v_pk_mul_f32 v[58:59], v[222:223], v[58:59] op_sel_hi:[0,1]
	v_pk_mul_f32 v[58:59], v[156:157], v[58:59]
	v_pk_fma_f32 v[58:59], v[244:245], s[12:13], v[58:59] op_sel_hi:[1,0,1]
	v_pk_mul_f32 v[60:61], v[222:223], v[60:61] op_sel_hi:[0,1]
	v_pk_mul_f32 v[60:61], v[158:159], v[60:61]
	v_pk_fma_f32 v[60:61], v[246:247], s[12:13], v[60:61] op_sel_hi:[1,0,1]
	v_cvt_pk_bf16_f32 v62, v62, v63
	v_cvt_pk_bf16_f32 v63, v64, v65
	v_cvt_pk_bf16_f32 v64, v58, v59
	v_cvt_pk_bf16_f32 v65, v60, v61
	v_add_u32_e32 v249, 0x50000, v249
	global_store_dwordx4 v249, v[62:65], s[6:7]
	global_load_dwordx4 v[240:243], v248, s[36:37] offset:512
	global_load_dwordx4 v[244:247], v248, s[36:37] offset:528
	v_cvt_f32_i32_e32 v54, v54
	v_cvt_f32_i32_e32 v55, v55
	v_cvt_f32_i32_e32 v56, v56
	v_cvt_f32_i32_e32 v57, v57
	v_cvt_f32_i32_e32 v50, v50
	v_cvt_f32_i32_e32 v51, v51
	v_cvt_f32_i32_e32 v52, v52
	v_cvt_f32_i32_e32 v53, v53
	s_waitcnt vmcnt(6)
	v_pk_mul_f32 v[54:55], v[222:223], v[54:55] op_sel_hi:[0,1]
	v_pk_mul_f32 v[54:55], v[160:161], v[54:55]
	v_pk_fma_f32 v[54:55], v[224:225], s[12:13], v[54:55] op_sel_hi:[1,0,1]
	v_pk_mul_f32 v[56:57], v[222:223], v[56:57] op_sel_hi:[0,1]
	v_pk_mul_f32 v[56:57], v[162:163], v[56:57]
	v_pk_fma_f32 v[56:57], v[226:227], s[12:13], v[56:57] op_sel_hi:[1,0,1]
	v_pk_mul_f32 v[50:51], v[222:223], v[50:51] op_sel_hi:[0,1]
	v_pk_mul_f32 v[50:51], v[164:165], v[50:51]
	v_pk_fma_f32 v[50:51], v[228:229], s[12:13], v[50:51] op_sel_hi:[1,0,1]
	v_pk_mul_f32 v[52:53], v[222:223], v[52:53] op_sel_hi:[0,1]
	v_pk_mul_f32 v[52:53], v[166:167], v[52:53]
	v_pk_fma_f32 v[52:53], v[230:231], s[12:13], v[52:53] op_sel_hi:[1,0,1]
	v_cvt_pk_bf16_f32 v54, v54, v55
	v_cvt_pk_bf16_f32 v55, v56, v57
	v_cvt_pk_bf16_f32 v56, v50, v51
	v_cvt_pk_bf16_f32 v57, v52, v53
	global_store_dwordx4 v249, v[54:57], s[6:7] offset:256
	v_add_u32_e32 v248, 0x20000, v248
	global_load_dwordx4 v[224:227], v248, s[36:37]
	global_load_dwordx4 v[228:231], v248, s[36:37] offset:16
	v_cvt_f32_i32_e32 v46, v46
	v_cvt_f32_i32_e32 v47, v47
	v_cvt_f32_i32_e32 v48, v48
	v_cvt_f32_i32_e32 v49, v49
	v_cvt_f32_i32_e32 v42, v42
	v_cvt_f32_i32_e32 v43, v43
	v_cvt_f32_i32_e32 v44, v44
	v_cvt_f32_i32_e32 v45, v45
	s_waitcnt vmcnt(6)
	v_mul_f32_e32 v222, 0x3a124925, v173
	v_pk_mul_f32 v[46:47], v[222:223], v[46:47] op_sel_hi:[0,1]
	v_pk_mul_f32 v[46:47], v[152:153], v[46:47]
	v_pk_fma_f32 v[46:47], v[232:233], s[12:13], v[46:47] op_sel_hi:[1,0,1]
	v_pk_mul_f32 v[48:49], v[222:223], v[48:49] op_sel_hi:[0,1]
	v_pk_mul_f32 v[48:49], v[154:155], v[48:49]
	v_pk_fma_f32 v[48:49], v[234:235], s[12:13], v[48:49] op_sel_hi:[1,0,1]
	v_pk_mul_f32 v[42:43], v[222:223], v[42:43] op_sel_hi:[0,1]
	v_pk_mul_f32 v[42:43], v[156:157], v[42:43]
	v_pk_fma_f32 v[42:43], v[236:237], s[12:13], v[42:43] op_sel_hi:[1,0,1]
	v_pk_mul_f32 v[44:45], v[222:223], v[44:45] op_sel_hi:[0,1]
	v_pk_mul_f32 v[44:45], v[158:159], v[44:45]
	v_pk_fma_f32 v[44:45], v[238:239], s[12:13], v[44:45] op_sel_hi:[1,0,1]
	v_cvt_pk_bf16_f32 v46, v46, v47
	v_cvt_pk_bf16_f32 v47, v48, v49
	v_cvt_pk_bf16_f32 v48, v42, v43
	v_cvt_pk_bf16_f32 v49, v44, v45
	v_add_u32_e32 v249, 0x10000, v249
	global_store_dwordx4 v249, v[46:49], s[6:7]
	global_load_dwordx4 v[232:235], v248, s[36:37] offset:512
	global_load_dwordx4 v[236:239], v248, s[36:37] offset:528
	v_cvt_f32_i32_e32 v38, v38
	v_cvt_f32_i32_e32 v39, v39
	v_cvt_f32_i32_e32 v40, v40
	v_cvt_f32_i32_e32 v41, v41
	v_cvt_f32_i32_e32 v34, v34
	v_cvt_f32_i32_e32 v35, v35
	v_cvt_f32_i32_e32 v36, v36
	v_cvt_f32_i32_e32 v37, v37
	s_waitcnt vmcnt(6)
	v_pk_mul_f32 v[38:39], v[222:223], v[38:39] op_sel_hi:[0,1]
	v_pk_mul_f32 v[38:39], v[160:161], v[38:39]
	v_pk_fma_f32 v[38:39], v[240:241], s[12:13], v[38:39] op_sel_hi:[1,0,1]
	v_pk_mul_f32 v[40:41], v[222:223], v[40:41] op_sel_hi:[0,1]
	v_pk_mul_f32 v[40:41], v[162:163], v[40:41]
	v_pk_fma_f32 v[40:41], v[242:243], s[12:13], v[40:41] op_sel_hi:[1,0,1]
	v_pk_mul_f32 v[34:35], v[222:223], v[34:35] op_sel_hi:[0,1]
	v_pk_mul_f32 v[34:35], v[164:165], v[34:35]
	v_pk_fma_f32 v[34:35], v[244:245], s[12:13], v[34:35] op_sel_hi:[1,0,1]
	v_pk_mul_f32 v[36:37], v[222:223], v[36:37] op_sel_hi:[0,1]
	v_pk_mul_f32 v[36:37], v[166:167], v[36:37]
	v_pk_fma_f32 v[36:37], v[246:247], s[12:13], v[36:37] op_sel_hi:[1,0,1]
	v_cvt_pk_bf16_f32 v38, v38, v39
	v_cvt_pk_bf16_f32 v39, v40, v41
	v_cvt_pk_bf16_f32 v40, v34, v35
	v_cvt_pk_bf16_f32 v41, v36, v37
	global_store_dwordx4 v249, v[38:41], s[6:7] offset:256
	v_add_u32_e32 v248, 0x20000, v248
	global_load_dwordx4 v[240:243], v248, s[36:37]
	global_load_dwordx4 v[244:247], v248, s[36:37] offset:16
	v_cvt_f32_i32_e32 v30, v30
	v_cvt_f32_i32_e32 v31, v31
	v_cvt_f32_i32_e32 v32, v32
	v_cvt_f32_i32_e32 v33, v33
	v_cvt_f32_i32_e32 v26, v26
	v_cvt_f32_i32_e32 v27, v27
	v_cvt_f32_i32_e32 v28, v28
	v_cvt_f32_i32_e32 v29, v29
	s_waitcnt vmcnt(6)
	v_mul_f32_e32 v222, 0x3a124925, v174
	v_pk_mul_f32 v[30:31], v[222:223], v[30:31] op_sel_hi:[0,1]
	v_pk_mul_f32 v[30:31], v[152:153], v[30:31]
	v_pk_fma_f32 v[30:31], v[224:225], s[12:13], v[30:31] op_sel_hi:[1,0,1]
	v_pk_mul_f32 v[32:33], v[222:223], v[32:33] op_sel_hi:[0,1]
	v_pk_mul_f32 v[32:33], v[154:155], v[32:33]
	v_pk_fma_f32 v[32:33], v[226:227], s[12:13], v[32:33] op_sel_hi:[1,0,1]
	v_pk_mul_f32 v[26:27], v[222:223], v[26:27] op_sel_hi:[0,1]
	v_pk_mul_f32 v[26:27], v[156:157], v[26:27]
	v_pk_fma_f32 v[26:27], v[228:229], s[12:13], v[26:27] op_sel_hi:[1,0,1]
	v_pk_mul_f32 v[28:29], v[222:223], v[28:29] op_sel_hi:[0,1]
	v_pk_mul_f32 v[28:29], v[158:159], v[28:29]
	v_pk_fma_f32 v[28:29], v[230:231], s[12:13], v[28:29] op_sel_hi:[1,0,1]
	v_cvt_pk_bf16_f32 v30, v30, v31
	v_cvt_pk_bf16_f32 v31, v32, v33
	v_cvt_pk_bf16_f32 v32, v26, v27
	v_cvt_pk_bf16_f32 v33, v28, v29
	v_add_u32_e32 v249, 0x10000, v249
	global_store_dwordx4 v249, v[30:33], s[6:7]
	global_load_dwordx4 v[224:227], v248, s[36:37] offset:512
	global_load_dwordx4 v[228:231], v248, s[36:37] offset:528
	v_cvt_f32_i32_e32 v22, v22
	v_cvt_f32_i32_e32 v23, v23
	v_cvt_f32_i32_e32 v24, v24
	v_cvt_f32_i32_e32 v25, v25
	v_cvt_f32_i32_e32 v18, v18
	v_cvt_f32_i32_e32 v19, v19
	v_cvt_f32_i32_e32 v20, v20
	v_cvt_f32_i32_e32 v21, v21
	s_waitcnt vmcnt(6)
	v_pk_mul_f32 v[22:23], v[222:223], v[22:23] op_sel_hi:[0,1]
	v_pk_mul_f32 v[22:23], v[160:161], v[22:23]
	v_pk_fma_f32 v[22:23], v[232:233], s[12:13], v[22:23] op_sel_hi:[1,0,1]
	v_pk_mul_f32 v[24:25], v[222:223], v[24:25] op_sel_hi:[0,1]
	v_pk_mul_f32 v[24:25], v[162:163], v[24:25]
	v_pk_fma_f32 v[24:25], v[234:235], s[12:13], v[24:25] op_sel_hi:[1,0,1]
	v_pk_mul_f32 v[18:19], v[222:223], v[18:19] op_sel_hi:[0,1]
	v_pk_mul_f32 v[18:19], v[164:165], v[18:19]
	v_pk_fma_f32 v[18:19], v[236:237], s[12:13], v[18:19] op_sel_hi:[1,0,1]
	v_pk_mul_f32 v[20:21], v[222:223], v[20:21] op_sel_hi:[0,1]
	v_pk_mul_f32 v[20:21], v[166:167], v[20:21]
	v_pk_fma_f32 v[20:21], v[238:239], s[12:13], v[20:21] op_sel_hi:[1,0,1]
	v_cvt_pk_bf16_f32 v22, v22, v23
	v_cvt_pk_bf16_f32 v23, v24, v25
	v_cvt_pk_bf16_f32 v24, v18, v19
	v_cvt_pk_bf16_f32 v25, v20, v21
	global_store_dwordx4 v249, v[22:25], s[6:7] offset:256
	v_cvt_f32_i32_e32 v14, v14
	v_cvt_f32_i32_e32 v15, v15
	v_cvt_f32_i32_e32 v16, v16
	v_cvt_f32_i32_e32 v17, v17
	v_cvt_f32_i32_e32 v10, v10
	v_cvt_f32_i32_e32 v11, v11
	v_cvt_f32_i32_e32 v12, v12
	v_cvt_f32_i32_e32 v13, v13
	s_waitcnt vmcnt(4)
	v_mul_f32_e32 v222, 0x3a124925, v175
	v_pk_mul_f32 v[14:15], v[222:223], v[14:15] op_sel_hi:[0,1]
	v_pk_mul_f32 v[14:15], v[152:153], v[14:15]
	v_pk_fma_f32 v[14:15], v[240:241], s[12:13], v[14:15] op_sel_hi:[1,0,1]
	v_pk_mul_f32 v[16:17], v[222:223], v[16:17] op_sel_hi:[0,1]
	v_pk_mul_f32 v[16:17], v[154:155], v[16:17]
	v_pk_fma_f32 v[16:17], v[242:243], s[12:13], v[16:17] op_sel_hi:[1,0,1]
	v_pk_mul_f32 v[10:11], v[222:223], v[10:11] op_sel_hi:[0,1]
	v_pk_mul_f32 v[10:11], v[156:157], v[10:11]
	v_pk_fma_f32 v[10:11], v[244:245], s[12:13], v[10:11] op_sel_hi:[1,0,1]
	v_pk_mul_f32 v[12:13], v[222:223], v[12:13] op_sel_hi:[0,1]
	v_pk_mul_f32 v[12:13], v[158:159], v[12:13]
	v_pk_fma_f32 v[12:13], v[246:247], s[12:13], v[12:13] op_sel_hi:[1,0,1]
	v_cvt_pk_bf16_f32 v14, v14, v15
	v_cvt_pk_bf16_f32 v15, v16, v17
	v_cvt_pk_bf16_f32 v16, v10, v11
	v_cvt_pk_bf16_f32 v17, v12, v13
	v_add_u32_e32 v249, 0x10000, v249
	global_store_dwordx4 v249, v[14:17], s[6:7]
	v_cvt_f32_i32_e32 v6, v6
	v_cvt_f32_i32_e32 v7, v7
	v_cvt_f32_i32_e32 v8, v8
	v_cvt_f32_i32_e32 v9, v9
	v_cvt_f32_i32_e32 v2, v2
	v_cvt_f32_i32_e32 v3, v3
	v_cvt_f32_i32_e32 v4, v4
	v_cvt_f32_i32_e32 v5, v5
	s_waitcnt vmcnt(2)
	v_pk_mul_f32 v[6:7], v[222:223], v[6:7] op_sel_hi:[0,1]
	v_pk_mul_f32 v[6:7], v[160:161], v[6:7]
	v_pk_fma_f32 v[6:7], v[224:225], s[12:13], v[6:7] op_sel_hi:[1,0,1]
	v_pk_mul_f32 v[8:9], v[222:223], v[8:9] op_sel_hi:[0,1]
	v_pk_mul_f32 v[8:9], v[162:163], v[8:9]
	v_pk_fma_f32 v[8:9], v[226:227], s[12:13], v[8:9] op_sel_hi:[1,0,1]
	v_pk_mul_f32 v[2:3], v[222:223], v[2:3] op_sel_hi:[0,1]
	v_pk_mul_f32 v[2:3], v[164:165], v[2:3]
	v_pk_fma_f32 v[2:3], v[228:229], s[12:13], v[2:3] op_sel_hi:[1,0,1]
	v_pk_mul_f32 v[4:5], v[222:223], v[4:5] op_sel_hi:[0,1]
	v_pk_mul_f32 v[4:5], v[166:167], v[4:5]
	v_pk_fma_f32 v[4:5], v[230:231], s[12:13], v[4:5] op_sel_hi:[1,0,1]
	v_cvt_pk_bf16_f32 v6, v6, v7
	v_cvt_pk_bf16_f32 v7, v8, v9
	v_cvt_pk_bf16_f32 v8, v2, v3
	v_cvt_pk_bf16_f32 v9, v4, v5
	global_store_dwordx4 v249, v[6:9], s[6:7] offset:256
	s_mov_b64 s[28:29], s[22:23]
	s_mov_b64 s[26:27], s[20:21]
	s_and_b64 vcc, exec, s[18:19]
	s_mov_b32 s24, s14
	s_mov_b32 s4, s16
	s_cbranch_vccz .LBB0_680
	s_waitcnt vmcnt(0)
	s_cmpk_gt_u32 s13, 0xff
	s_cbranch_scc1 .LBB0_688
	s_barrier
